# also the GQA leading-half unit prologue: vmcnt(0) drain between LDS-DMA issues removed
# baseline (speedup 1.0000x reference)
; #define ATT_DMA_K(t, sl) do { glds16(ksrc + (size_t)(t) * 64 * kpitch, (unsigned)__builtin_amdgcn_readfirstlane(kdst + (sl) * KSLOT)); \
;         if constexpr (DQK == 96) glds16(krsrc + (size_t)(t) * 64 * 32, (unsigned)__builtin_amdgcn_readfirstlane(krdst + (sl) * KSLOT)); } while (0)
; #define ATT_DMA_V(t, sl) do { glds16(vsrc + (size_t)(t) * 64, (unsigned)__builtin_amdgcn_readfirstlane(vdst + (sl) * VSLOT)); \
;         if constexpr (DV == 128) glds16(vsrc + (size_t)64 * NR + (size_t)(t) * 64, (unsigned)__builtin_amdgcn_readfirstlane(vdst + (sl) * VSLOT + 8192)); } while (0)
; template <int DQK, int DV, bool LEAD> ...
;     ...
;     ATT_DMA_K(0, 0); ATT_DMA_V(0, 0); ATT_DMA_K(1, 1); ATT_DMA_K(2, 2);
;     bf16x8 qf[NQB * NDS];
;     {
;       const float c2 = (DQK == 64) ? C2_EVEN : C2_ODD; const bool lat = tq0 >= 0;
; #pragma unroll
;       for (int qb = 0; qb < NQB; ++qb) {
;           const bf16_t* qp = Q + (size_t)(qrow0 + qoff + qb * 16 + q16) * qpitch + g4 * 8;
;           bf16x8 raw[NDS];
; #pragma unroll
;           for (int ds = 0; ds < NDS; ++ds) raw[ds] = *(const bf16x8*)(qp + ds * 32);
;           float x[NDS][8];
; #pragma unroll
;           for (int ds = 0; ds < NDS; ++ds)
; #pragma unroll
;               for (int j = 0; j < 8; ++j) x[ds][j] = __uint_as_float(((unsigned)(unsigned short)raw[ds][j]) << 16);
;           const int tq = tq0 + qoff + qb * 16 + q16, prow = (tq >> 6) & 127, pcol = tq & 63;
;           float sn = 0.f;
; #pragma unroll
;           for (int ds = 0; ds < 2; ++ds)
; #pragma unroll
;               for (int j = 0; j < 8; ++j) sn += x[ds][j] * x[ds][j];
;           sn = lanes4_sum(sn);
;           const float rn = rsqrtf(sn * (1.f / 64.f) + EPS);
; #pragma unroll
;           for (int ds = 0; ds < 2; ++ds)
; #pragma unroll
;               for (int j = 0; j < 8; ++j) x[ds][j] *= rn * qgain[32 * ds + 8 * g4 + j];
.LBB0_962:
	s_and_b64 vcc, exec, s[4:5]
	s_cbranch_vccz .LBB0_954
	v_mov_b32_e32 v168, v0
	s_ashr_i32 s45, s44, 31
	v_readfirstlane_b32 s16, v168
	s_ashr_i32 s4, s16, 6
	v_bfe_u32 v1, v168, 3, 3
	v_lshl_or_b32 v7, s4, 3, v1
	s_lshl_b32 s5, s4, 1
	s_lshr_b32 s6, s16, 5
	v_ashrrev_i32_e32 v2, 1, v7
	s_and_b32 s5, s5, 2
	s_and_b32 s6, s6, 4
	v_and_b32_e32 v170, 7, v168
	v_and_b32_e32 v3, 1, v2
	s_or_b32 s5, s5, s6
	s_and_b32 s7, s4, 3
	v_bitop3_b32 v8, s5, v170, v3 bitop3:0x36
	v_xor_b32_e32 v9, v2, v168
	v_add_u32_e32 v4, s44, v7
	s_lshl_b32 s4, s4, 10
	v_mov_b64_e32 v[2:3], s[36:37]
	s_add_i32 s49, s4, 0
	v_mad_i64_i32 v[2:3], s[4:5], v4, s92, v[2:3]
	v_mov_b64_e32 v[4:5], s[40:41]
	v_lshlrev_b32_e32 v194, 4, v8
	v_mad_i64_i32 v[4:5], s[4:5], v7, s91, v[4:5]
	v_lshl_add_u64 v[162:163], v[2:3], 0, v[194:195]
	v_lshlrev_b32_e32 v2, 4, v9
	v_lshl_add_u64 v[4:5], s[44:45], 1, v[4:5]
	v_and_b32_e32 v194, 0x70, v2
	s_mov_b32 s4, m0
	s_mov_b32 m0, s49
	s_nop 0
	global_load_lds_dwordx4 v[162:163], off
	s_mov_b32 m0, s4
	v_lshl_add_u64 v[164:165], v[4:5], 0, v[194:195]
	s_add_i32 s36, s49, 0x9000
	s_mov_b32 s4, m0
	s_mov_b32 m0, s36
	s_nop 0
	global_load_lds_dwordx4 v[164:165], off
	s_mov_b32 m0, s4
	s_mov_b64 s[4:5], 0x38000
	s_lshl_b32 s37, s7, 6
	v_lshl_add_u64 v[2:3], v[162:163], 0, s[4:5]
	s_add_i32 s4, s49, 0x2000
	s_mov_b32 s5, m0
	s_mov_b32 m0, s4
	s_nop 0
	global_load_lds_dwordx4 v[2:3], off
	s_mov_b32 m0, s5
	v_and_b32_e32 v6, 15, v168
	s_mov_b64 s[4:5], 0x70000
	s_or_b32 s6, s37, s48
	v_and_b32_e32 v194, 48, v168
	v_lshrrev_b32_e32 v40, 1, v168
	v_lshlrev_b32_e32 v173, 7, v6
	v_lshl_add_u64 v[2:3], v[162:163], 0, s[4:5]
	s_add_i32 s4, s49, 0x4000
	v_or_b32_e32 v22, s6, v6
	v_lshl_add_u64 v[6:7], s[28:29], 0, v[194:195]
	s_mov_b32 s5, m0
	s_mov_b32 m0, s4
	s_nop 0
	global_load_lds_dwordx4 v[2:3], off
	s_mov_b32 m0, s5
	v_and_b32_e32 v41, 8, v40
	v_mad_i64_i32 v[8:9], s[4:5], v22, s92, v[6:7]
	v_or_b32_e32 v10, 16, v22
	v_or_b32_e32 v18, 32, v22
	v_or_b32_e32 v22, 48, v22
	v_lshl_or_b32 v194, v41, 3, v173
	v_mad_i64_i32 v[16:17], s[4:5], v10, s92, v[6:7]
	v_mad_i64_i32 v[18:19], s[4:5], v18, s92, v[6:7]
	v_mad_i64_i32 v[34:35], s[4:5], v22, s92, v[6:7]
	v_lshl_add_u64 v[14:15], s[8:9], 0, v[194:195]
	s_mov_b64 s[4:5], 0x1800
	v_lshl_add_u64 v[36:37], v[14:15], 0, s[4:5]
	s_movk_i32 s4, 0x1000
	v_add_co_u32_e32 v38, vcc, s4, v14
	global_load_dwordx4 v[2:5], v194, s[8:9] offset:48
	v_lshl_add_u64 v[20:21], v[14:15], 0, s[60:61]
	v_addc_co_u32_e32 v39, vcc, 0, v15, vcc
	global_load_dwordx4 v[74:77], v[8:9], off offset:64
	global_load_dwordx4 v[124:127], v[16:17], off offset:64
	global_load_dwordx4 v[10:13], v194, s[8:9] offset:2096
	global_load_dwordx4 v[142:145], v[18:19], off offset:64
	global_load_dwordx4 v[70:73], v[20:21], off offset:48
	global_load_dwordx4 v[154:157], v[34:35], off offset:64
	global_load_dwordx4 v[26:29], v[36:37], off offset:48
	global_load_dwordx4 v[100:103], v194, s[8:9] offset:32
	global_load_dwordx4 v[92:95], v194, s[8:9] offset:2080
	global_load_dwordx4 v[66:69], v[20:21], off offset:32
	global_load_dwordx4 v[30:33], v[36:37], off offset:32
	global_load_dwordx4 v[108:111], v[8:9], off
	s_nop 0
	global_load_dwordx4 v[6:9], v194, s[8:9]
	global_load_dwordx4 v[104:107], v[16:17], off
	global_load_dwordx4 v[96:99], v194, s[8:9] offset:16
	global_load_dwordx4 v[80:83], v[18:19], off
	global_load_dwordx4 v[84:87], v194, s[8:9] offset:2064
	global_load_dwordx4 v[22:25], v[38:39], off
	s_nop 0
	global_load_dwordx4 v[14:17], v[34:35], off
	global_load_dwordx4 v[88:91], v194, s[8:9] offset:2048
	s_lshl_b32 s4, s16, 4
	global_load_dwordx4 v[18:21], v[20:21], off offset:16
	v_lshlrev_b32_e32 v172, 1, v168
	v_and_b32_e32 v34, 3, v168
	s_and_b32 s4, s4, 0xfffff000
	v_and_or_b32 v42, v172, 24, v34
	s_add_i32 s4, s4, 0
	v_lshl_add_u32 v169, v42, 7, s4
	s_or_b32 s4, s47, s37
	v_bfe_u32 v171, v168, 4, 2
	s_lshr_b32 s4, s4, 2
	v_bitop3_b32 v40, v171, v40, 7 bitop3:0x78
	s_and_b32 s4, s4, 0x7f0
	v_lshlrev_b32_e32 v177, 4, v40
	v_or_b32_e32 v40, s4, v41
	v_lshlrev_b32_e32 v40, 3, v40
	global_load_dwordx4 v[34:37], v[36:37], off offset:16
	v_lshlrev_b32_e32 v78, 5, v171
	global_load_dwordx4 v[42:45], v40, s[8:9] offset:48
	global_load_dwordx4 v[46:49], v40, s[8:9] offset:32
	global_load_dwordx4 v[50:53], v40, s[8:9] offset:16
	global_load_dwordx4 v[54:57], v40, s[8:9]
	s_nop 0
	global_load_dwordx4 v[38:41], v[38:39], off offset:2048
	s_nop 0
	global_load_dwordx4 v[58:61], v78, s[26:27] offset:144
	global_load_dwordx4 v[62:65], v78, s[26:27] offset:128
	v_and_b32_e32 v174, 63, v168
	v_cmp_gt_u32_e32 vcc, 32, v174
	s_mov_b32 s4, 0x358637bd
	s_mov_b32 s12, 0x3c800000
	v_add_u32_e32 v175, v169, v177
	s_mov_b32 s28, 1
	v_or_b32_e32 v176, 4, v171
	s_mov_b32 s29, 0
	s_waitcnt vmcnt(22)
	v_cndmask_b32_e64 v113, v29, -v29, vcc
	v_cndmask_b32_e64 v146, v3, -v3, vcc
	v_mov_b32_e32 v3, v4
	v_cndmask_b32_e64 v147, v5, -v5, vcc
	s_waitcnt vmcnt(20)
	v_cndmask_b32_e64 v133, v95, -v95, vcc
	s_waitcnt vmcnt(17)
	v_and_b32_e32 v181, 0xffff0000, v108
	v_lshlrev_b32_e32 v180, 16, v108
	v_mul_f32_e32 v4, v181, v181
	v_and_b32_e32 v131, 0xffff0000, v127
	v_lshlrev_b32_e32 v130, 16, v127
	v_cndmask_b32_e64 v129, v13, -v13, vcc
	v_cndmask_b32_e64 v128, v11, -v11, vcc
	v_mov_b32_e32 v11, v12
	v_and_b32_e32 v119, 0xffff0000, v145
	v_lshlrev_b32_e32 v118, 16, v145
	v_and_b32_e32 v115, 0xffff0000, v157
	v_lshlrev_b32_e32 v114, 16, v157
	v_cndmask_b32_e64 v13, v103, -v103, vcc
	v_cndmask_b32_e64 v12, v101, -v101, vcc
	v_mov_b32_e32 v101, v102
	v_and_b32_e32 v135, 0xffff0000, v126
	v_lshlrev_b32_e32 v134, 16, v126
	v_cndmask_b32_e64 v132, v93, -v93, vcc
	v_mov_b32_e32 v93, v94
	v_and_b32_e32 v103, 0xffff0000, v144
	v_lshlrev_b32_e32 v102, 16, v144
	v_cndmask_b32_e64 v95, v69, -v69, vcc
	v_cndmask_b32_e64 v94, v67, -v67, vcc
	v_mov_b32_e32 v67, v68
	v_and_b32_e32 v69, 0xffff0000, v156
	v_lshlrev_b32_e32 v68, 16, v156
	s_waitcnt vmcnt(14)
; template <int DQK, int DV, bool LEAD> ...
;     ...
;           const bf16_t* qp = Q + (size_t)(qrow0 + qoff + qb * 16 + q16) * qpitch + g4 * 8;
;           bf16x8 raw[NDS];
; #pragma unroll
;           for (int ds = 0; ds < NDS; ++ds) raw[ds] = *(const bf16x8*)(qp + ds * 32);
;           float x[NDS][8];
; #pragma unroll
;           for (int ds = 0; ds < NDS; ++ds)
; #pragma unroll
;               for (int j = 0; j < 8; ++j) x[ds][j] = __uint_as_float(((unsigned)(unsigned short)raw[ds][j]) << 16);
;           const int tq = tq0 + qoff + qb * 16 + q16, prow = (tq >> 6) & 127, pcol = tq & 63;
;           float sn = 0.f;
; #pragma unroll
;           for (int ds = 0; ds < 2; ++ds)
; #pragma unroll
;               for (int j = 0; j < 8; ++j) sn += x[ds][j] * x[ds][j];
;           sn = lanes4_sum(sn);
;           const float rn = rsqrtf(sn * (1.f / 64.f) + EPS);
; #pragma unroll
;           for (int ds = 0; ds < 2; ++ds)
; #pragma unroll
;               for (int j = 0; j < 8; ++j) x[ds][j] *= rn * qgain[32 * ds + 8 * g4 + j];
	v_cndmask_b32_e64 v157, v99, -v99, vcc
	v_cndmask_b32_e64 v156, v97, -v97, vcc
	v_mov_b32_e32 v97, v98
	v_and_b32_e32 v139, 0xffff0000, v125
	v_lshlrev_b32_e32 v138, 16, v125
	v_and_b32_e32 v123, 0xffff0000, v143
	v_lshlrev_b32_e32 v122, 16, v143
	v_and_b32_e32 v141, 0xffff0000, v124
	v_lshlrev_b32_e32 v140, 16, v124
	v_and_b32_e32 v127, 0xffff0000, v142
	v_lshlrev_b32_e32 v126, 16, v142
	s_waitcnt vmcnt(11)
	v_cndmask_b32_e64 v125, v25, -v25, vcc
	v_cndmask_b32_e64 v124, v23, -v23, vcc
	v_mov_b32_e32 v23, v24
	v_and_b32_e32 v143, 0xffff0000, v107
	v_lshlrev_b32_e32 v142, 16, v107
	v_and_b32_e32 v25, 0xffff0000, v83
	v_lshlrev_b32_e32 v24, 16, v83
	s_waitcnt vmcnt(10)
	v_and_b32_e32 v99, 0xffff0000, v17
	v_lshlrev_b32_e32 v98, 16, v17
	v_and_b32_e32 v145, 0xffff0000, v106
	v_lshlrev_b32_e32 v144, 16, v106
	v_and_b32_e32 v107, 0xffff0000, v82
	v_lshlrev_b32_e32 v106, 16, v82
	v_and_b32_e32 v83, 0xffff0000, v16
	v_lshlrev_b32_e32 v82, 16, v16
	v_and_b32_e32 v17, 0xffff0000, v109
	v_lshlrev_b32_e32 v16, 16, v109
	v_pk_fma_f32 v[4:5], v[180:181], v[180:181], v[4:5] op_sel_hi:[1,1,0]
	v_and_b32_e32 v151, 0xffff0000, v77
	v_lshlrev_b32_e32 v150, 16, v77
	v_cndmask_b32_e64 v117, v73, -v73, vcc
	v_cndmask_b32_e64 v116, v71, -v71, vcc
	v_mov_b32_e32 v71, v72
	v_and_b32_e32 v153, 0xffff0000, v76
	v_lshlrev_b32_e32 v152, 16, v76
	v_and_b32_e32 v159, 0xffff0000, v75
	v_lshlrev_b32_e32 v158, 16, v75
	v_and_b32_e32 v167, 0xffff0000, v74
	v_lshlrev_b32_e32 v166, 16, v74
	global_load_dwordx4 v[72:75], v78, s[26:27] offset:16
	s_nop 0
	global_load_dwordx4 v[76:79], v78, s[26:27]
	v_pk_fma_f32 v[4:5], v[16:17], v[16:17], v[4:5]
	v_mul_f32_e32 v108, v17, v17
	v_and_b32_e32 v179, 0xffff0000, v110
	v_lshlrev_b32_e32 v178, 16, v110
	v_pk_add_f32 v[4:5], v[108:109], v[4:5] op_sel_hi:[0,1]
	v_pk_fma_f32 v[4:5], v[178:179], v[178:179], v[4:5]
	v_mul_f32_e32 v108, v179, v179
	v_cndmask_b32_e64 v161, v9, -v9, vcc
	v_cndmask_b32_e64 v160, v7, -v7, vcc
	v_mov_b32_e32 v7, v8
	v_and_b32_e32 v9, 0xffff0000, v111
	v_lshlrev_b32_e32 v8, 16, v111
	v_pk_add_f32 v[4:5], v[108:109], v[4:5] op_sel_hi:[0,1]
	v_pk_fma_f32 v[4:5], v[8:9], v[8:9], v[4:5]
	v_mul_f32_e32 v108, v9, v9
	v_pk_add_f32 v[4:5], v[108:109], v[4:5] op_sel_hi:[0,1]
	v_pk_fma_f32 v[4:5], v[166:167], v[166:167], v[4:5]
	v_mul_f32_e32 v108, v167, v167
	v_pk_add_f32 v[4:5], v[108:109], v[4:5] op_sel_hi:[0,1]
	v_pk_fma_f32 v[4:5], v[158:159], v[158:159], v[4:5]
	v_mul_f32_e32 v108, v159, v159
	v_pk_add_f32 v[4:5], v[108:109], v[4:5] op_sel_hi:[0,1]
	v_pk_fma_f32 v[4:5], v[152:153], v[152:153], v[4:5]
	v_mul_f32_e32 v108, v153, v153
	v_pk_add_f32 v[4:5], v[108:109], v[4:5] op_sel_hi:[0,1]
	v_pk_fma_f32 v[4:5], v[150:151], v[150:151], v[4:5]
	v_mul_f32_e32 v108, v151, v151
	v_pk_add_f32 v[4:5], v[108:109], v[4:5] op_sel_hi:[0,1]
	v_mov_b32_e32 v5, v4
	s_nop 1
	v_permlane16_swap_b32_e32 v4, v5
	v_add_f32_e32 v5, v4, v5
	v_cndmask_b32_e64 v137, v87, -v87, vcc
	v_cndmask_b32_e64 v136, v85, -v85, vcc
	v_mov_b32_e32 v85, v86
	v_and_b32_e32 v87, 0xffff0000, v155
	v_lshlrev_b32_e32 v86, 16, v155
	v_and_b32_e32 v149, 0xffff0000, v105
	v_lshlrev_b32_e32 v148, 16, v105
	v_mov_b32_e32 v105, v5
	v_and_b32_e32 v155, 0xffff0000, v104
	s_waitcnt vmcnt(10)
	v_cndmask_b32_e64 v121, v21, -v21, vcc
	v_cndmask_b32_e64 v120, v19, -v19, vcc
	v_mov_b32_e32 v19, v20
	v_cndmask_b32_e64 v21, v91, -v91, vcc
	v_cndmask_b32_e64 v20, v89, -v89, vcc
	v_mov_b32_e32 v89, v90
	v_and_b32_e32 v91, 0xffff0000, v154
	v_lshlrev_b32_e32 v90, 16, v154
	v_permlane32_swap_b32_e32 v5, v105
	v_lshlrev_b32_e32 v154, 16, v104
	v_mul_f32_e32 v4, v155, v155
	v_pk_fma_f32 v[108:109], v[154:155], v[154:155], v[4:5] op_sel_hi:[1,1,0]
	v_mul_f32_e32 v4, v149, v149
	v_pk_fma_f32 v[108:109], v[148:149], v[148:149], v[108:109]
	v_cndmask_b32_e64 v112, v27, -v27, vcc
	v_pk_add_f32 v[108:109], v[4:5], v[108:109] op_sel_hi:[0,1]
	v_pk_fma_f32 v[108:109], v[144:145], v[144:145], v[108:109]
	v_mul_f32_e32 v4, v145, v145
	v_pk_add_f32 v[108:109], v[4:5], v[108:109] op_sel_hi:[0,1]
	v_pk_fma_f32 v[108:109], v[142:143], v[142:143], v[108:109]
	v_mul_f32_e32 v4, v143, v143
	v_pk_add_f32 v[108:109], v[4:5], v[108:109] op_sel_hi:[0,1]
	v_pk_fma_f32 v[108:109], v[140:141], v[140:141], v[108:109]
	v_mul_f32_e32 v4, v141, v141
	v_pk_add_f32 v[108:109], v[4:5], v[108:109] op_sel_hi:[0,1]
	v_pk_fma_f32 v[108:109], v[138:139], v[138:139], v[108:109]
	v_mul_f32_e32 v4, v139, v139
	v_pk_add_f32 v[108:109], v[4:5], v[108:109] op_sel_hi:[0,1]
	v_pk_fma_f32 v[108:109], v[134:135], v[134:135], v[108:109]
	v_mul_f32_e32 v4, v135, v135
	v_pk_add_f32 v[108:109], v[4:5], v[108:109] op_sel_hi:[0,1]
	v_pk_fma_f32 v[108:109], v[130:131], v[130:131], v[108:109]
	v_mul_f32_e32 v4, v131, v131
	v_pk_add_f32 v[108:109], v[4:5], v[108:109] op_sel_hi:[0,1]
	v_mov_b32_e32 v4, v108
	s_nop 1
	v_permlane16_swap_b32_e32 v108, v4
	v_add_f32_e32 v4, v108, v4
	v_mov_b32_e32 v104, v4
	s_nop 1
	v_permlane32_swap_b32_e32 v4, v104
	v_pk_add_f32 v[4:5], v[4:5], v[104:105]
	v_mov_b64_e32 v[108:109], s[4:5]
	v_pk_fma_f32 v[182:183], v[4:5], s[12:13], v[108:109] op_sel_hi:[1,0,0]
	s_waitcnt vmcnt(5)
	v_cndmask_b32_e64 v104, v55, -v55, vcc
	v_mul_f32_e32 v4, 0x4b800000, v183
	v_cmp_gt_f32_e64 s[4:5], s95, v183
	v_mov_b32_e32 v55, v56
	v_mov_b32_e32 v27, v28
	v_cndmask_b32_e64 v4, v183, v4, s[4:5]
	v_rsq_f32_e32 v4, v4
	v_cndmask_b32_e64 v29, v33, -v33, vcc
	v_cndmask_b32_e64 v28, v31, -v31, vcc
	v_mov_b32_e32 v31, v32
	v_mul_f32_e32 v5, 0x45800000, v4
	v_cndmask_b32_e64 v56, v4, v5, s[4:5]
	s_waitcnt vmcnt(3)
; __device__ __forceinline__ unsigned cvtpk(float lo, float hi) { f32x2 v = {lo, hi}; bf16x2_t b = __builtin_convertvector(v, bf16x2_t); return __builtin_bit_cast(unsigned, b); }
; template <int DQK, int DV, bool LEAD> ...
;     ...
; #pragma unroll
;           for (int ds = 0; ds < 2; ++ds)
; #pragma unroll
;               for (int j = 0; j < 8; ++j) x[ds][j] *= rn * qgain[32 * ds + 8 * g4 + j];
;           if constexpr (DQK == 64) {
; #pragma unroll
;               for (int ds = 0; ds < 2; ++ds)
; #pragma unroll
;                   for (int j = 0; j < 8; ++j) {
;                       auto rr = __builtin_amdgcn_permlane32_swap(__float_as_uint(x[ds][j]), __float_as_uint(x[ds][j]), false, false);
;                       const float other = hi ? __uint_as_float(rr[0]) : __uint_as_float(rr[1]);
;                       float cc = 1.f, sg = 0.f;
;                       if (lat) { const f32x2 cs = rope[(ds ? pcol : prow) * 16 + 8 * (g4 & 1) + j]; cc = cs.x; sg = hi ? cs.y : -cs.y; }
;                       x[ds][j] = x[ds][j] * cc + other * sg; }
;     ...
; #pragma unroll
;           for (int ds = 0; ds < NDS; ++ds) { u32x4 w;
; #pragma unroll
;               for (int i = 0; i < 4; ++i) w[i] = cvtpk(x[ds][2 * i] * c2, x[ds][2 * i + 1] * c2);
;               qf[qb * NDS + ds] = __builtin_bit_cast(bf16x8, w); }
	v_pk_mul_f32 v[4:5], v[56:57], v[60:61] op_sel_hi:[0,1]
	v_pk_mul_f32 v[4:5], v[4:5], v[150:151]
	v_cndmask_b32_e64 v33, v37, -v37, vcc
	v_cndmask_b32_e64 v32, v35, -v35, vcc
	v_mov_b32_e32 v35, v36
	v_cndmask_b32_e64 v37, v41, -v41, vcc
	v_cndmask_b32_e64 v36, v39, -v39, vcc
	v_mov_b32_e32 v39, v40
	v_cndmask_b32_e64 v41, v45, -v45, vcc
	v_cndmask_b32_e64 v40, v43, -v43, vcc
	v_mov_b32_e32 v43, v44
	v_cndmask_b32_e64 v45, v49, -v49, vcc
	v_cndmask_b32_e64 v44, v47, -v47, vcc
	v_mov_b32_e32 v47, v48
	v_cndmask_b32_e64 v49, v53, -v53, vcc
	v_cndmask_b32_e64 v48, v51, -v51, vcc
	v_mov_b32_e32 v51, v52
	v_and_b32_e32 v111, 0xffff0000, v81
	v_lshlrev_b32_e32 v110, 16, v81
	v_and_b32_e32 v53, 0xffff0000, v15
	v_lshlrev_b32_e32 v52, 16, v15
	v_cndmask_b32_e64 v105, v57, -v57, vcc
	v_mov_b32_e32 v15, v4
	v_mov_b32_e32 v57, v4
	v_mov_b32_e32 v81, v5
	v_mov_b32_e32 v150, v5
	v_permlane32_swap_b32_e32 v15, v57
	s_nop 0
	v_permlane32_swap_b32_e32 v81, v150
	v_cndmask_b32_e32 v151, v81, v150, vcc
	v_cndmask_b32_e32 v150, v15, v57, vcc
	v_pk_mul_f32 v[146:147], v[146:147], v[150:151]
	v_cmp_gt_f32_e64 s[4:5], s95, v182
	v_pk_fma_f32 v[2:3], v[4:5], v[2:3], v[146:147]
	s_lshl_b32 s26, s46, 8
	v_pk_mul_f32 v[2:3], v[2:3], s[94:95] op_sel_hi:[1,0]
	s_cmpk_lt_u32 s16, 0x100
	v_cvt_pk_bf16_f32 v5, v2, v3
	v_pk_mul_f32 v[2:3], v[56:57], v[58:59] op_sel_hi:[0,1]
	v_pk_mul_f32 v[2:3], v[2:3], v[152:153]
	s_mov_b32 s27, 2
	v_mov_b32_e32 v4, v2
	v_mov_b32_e32 v15, v2
	v_mov_b32_e32 v57, v3
	v_mov_b32_e32 v81, v3
	v_permlane32_swap_b32_e32 v4, v15
	s_nop 0
	v_permlane32_swap_b32_e32 v57, v81
	v_cndmask_b32_e32 v147, v57, v81, vcc
	v_cndmask_b32_e32 v146, v4, v15, vcc
	v_pk_mul_f32 v[12:13], v[12:13], v[146:147]
	s_nop 0
	v_pk_fma_f32 v[2:3], v[2:3], v[100:101], v[12:13]
	s_nop 0
	v_pk_mul_f32 v[2:3], v[2:3], s[94:95] op_sel_hi:[1,0]
	s_nop 0
	v_cvt_pk_bf16_f32 v4, v2, v3
	s_waitcnt vmcnt(2)
	v_pk_mul_f32 v[2:3], v[56:57], v[64:65] op_sel_hi:[0,1]
	v_pk_mul_f32 v[2:3], v[2:3], v[158:159]
	s_nop 0
	v_mov_b32_e32 v12, v2
	v_mov_b32_e32 v15, v2
	v_mov_b32_e32 v13, v3
	v_mov_b32_e32 v57, v3
	v_permlane32_swap_b32_e32 v12, v15
	s_nop 0
	v_permlane32_swap_b32_e32 v13, v57
	v_cndmask_b32_e32 v13, v13, v57, vcc
	v_cndmask_b32_e32 v12, v12, v15, vcc
	v_pk_mul_f32 v[12:13], v[156:157], v[12:13]
	s_nop 0
	v_pk_fma_f32 v[2:3], v[2:3], v[96:97], v[12:13]
	v_pk_mul_f32 v[12:13], v[62:63], v[56:57] op_sel_hi:[1,0]
	v_pk_mul_f32 v[2:3], v[2:3], s[94:95] op_sel_hi:[1,0]
	v_pk_mul_f32 v[12:13], v[12:13], v[166:167]
	v_cvt_pk_bf16_f32 v3, v2, v3
	v_mov_b32_e32 v2, v12
	v_mov_b32_e32 v15, v12
	v_mov_b32_e32 v57, v13
	v_mov_b32_e32 v81, v13
	v_permlane32_swap_b32_e32 v2, v15
	s_nop 0
	v_permlane32_swap_b32_e32 v57, v81
	v_cndmask_b32_e32 v97, v57, v81, vcc
	v_cndmask_b32_e32 v96, v2, v15, vcc
	v_pk_mul_f32 v[96:97], v[160:161], v[96:97]
	s_nop 0
	v_pk_fma_f32 v[6:7], v[12:13], v[6:7], v[96:97]
	s_nop 0
	v_pk_mul_f32 v[6:7], v[6:7], s[94:95] op_sel_hi:[1,0]
	s_nop 0
	v_cvt_pk_bf16_f32 v2, v6, v7
	s_waitcnt vmcnt(1)
	v_pk_mul_f32 v[6:7], v[74:75], v[56:57] op_sel_hi:[1,0]
	s_nop 0
	v_pk_mul_f32 v[6:7], v[6:7], v[8:9]
	s_nop 0
	v_mov_b32_e32 v8, v6
	v_mov_b32_e32 v12, v6
	v_mov_b32_e32 v9, v7
	v_mov_b32_e32 v13, v7
	v_permlane32_swap_b32_e32 v8, v12
	s_nop 0
	v_permlane32_swap_b32_e32 v9, v13
	v_cndmask_b32_e32 v9, v9, v13, vcc
	v_cndmask_b32_e32 v8, v8, v12, vcc
	v_pk_mul_f32 v[8:9], v[40:41], v[8:9]
	s_nop 0
	v_pk_fma_f32 v[6:7], v[6:7], v[42:43], v[8:9]
	s_nop 0
	v_pk_mul_f32 v[6:7], v[6:7], s[94:95] op_sel_hi:[1,0]
	s_nop 0
	v_cvt_pk_bf16_f32 v9, v6, v7
	v_pk_mul_f32 v[6:7], v[72:73], v[56:57] op_sel_hi:[1,0]
	s_nop 0
	v_pk_mul_f32 v[6:7], v[6:7], v[178:179]
	s_nop 0
	v_mov_b32_e32 v8, v6
	v_mov_b32_e32 v12, v6
	v_mov_b32_e32 v13, v7
	v_mov_b32_e32 v15, v7
	v_permlane32_swap_b32_e32 v8, v12
	s_nop 0
	v_permlane32_swap_b32_e32 v13, v15
	v_cndmask_b32_e32 v13, v13, v15, vcc
	v_cndmask_b32_e32 v12, v8, v12, vcc
	v_pk_mul_f32 v[12:13], v[44:45], v[12:13]
	s_nop 0
	v_pk_fma_f32 v[6:7], v[6:7], v[46:47], v[12:13]
	s_nop 0
	v_pk_mul_f32 v[6:7], v[6:7], s[94:95] op_sel_hi:[1,0]
	s_nop 0
	v_cvt_pk_bf16_f32 v8, v6, v7
	s_waitcnt vmcnt(0)
	v_pk_mul_f32 v[6:7], v[78:79], v[56:57] op_sel_hi:[1,0]
	s_nop 0
	v_pk_mul_f32 v[6:7], v[6:7], v[16:17]
	s_nop 0
	v_mov_b32_e32 v12, v6
	v_mov_b32_e32 v15, v6
	v_mov_b32_e32 v13, v7
	v_mov_b32_e32 v16, v7
	v_permlane32_swap_b32_e32 v12, v15
	s_nop 0
	v_permlane32_swap_b32_e32 v13, v16
	v_cndmask_b32_e32 v13, v13, v16, vcc
	v_cndmask_b32_e32 v12, v12, v15, vcc
	v_pk_mul_f32 v[12:13], v[48:49], v[12:13]
	s_nop 0
	v_pk_fma_f32 v[6:7], v[6:7], v[50:51], v[12:13]
	v_pk_mul_f32 v[12:13], v[76:77], v[56:57] op_sel_hi:[1,0]
	v_pk_mul_f32 v[6:7], v[6:7], s[94:95] op_sel_hi:[1,0]
	v_pk_mul_f32 v[12:13], v[12:13], v[180:181]
	v_cvt_pk_bf16_f32 v7, v6, v7
	v_mov_b32_e32 v6, v12
	v_mov_b32_e32 v15, v12
	v_mov_b32_e32 v16, v13
	v_mov_b32_e32 v17, v13
	v_permlane32_swap_b32_e32 v6, v15
	s_nop 0
	v_permlane32_swap_b32_e32 v16, v17
	v_cndmask_b32_e32 v17, v16, v17, vcc
	v_cndmask_b32_e32 v16, v6, v15, vcc
	v_mul_f32_e32 v6, 0x4b800000, v182
	v_cndmask_b32_e64 v6, v182, v6, s[4:5]
	v_rsq_f32_e32 v15, v6
	v_pk_mul_f32 v[16:17], v[104:105], v[16:17]
	s_nop 0
	v_pk_fma_f32 v[12:13], v[12:13], v[54:55], v[16:17]
	s_nop 0
	v_pk_mul_f32 v[12:13], v[12:13], s[94:95] op_sel_hi:[1,0]
	s_nop 0
	v_cvt_pk_bf16_f32 v6, v12, v13
	v_mul_f32_e32 v12, 0x45800000, v15
	v_cndmask_b32_e64 v56, v15, v12, s[4:5]
	v_pk_mul_f32 v[12:13], v[60:61], v[56:57] op_sel_hi:[1,0]
	s_nop 0
	v_pk_mul_f32 v[12:13], v[12:13], v[130:131]
	s_nop 0
	v_mov_b32_e32 v15, v12
	v_mov_b32_e32 v16, v12
	v_mov_b32_e32 v17, v13
; __device__ __forceinline__ unsigned cvtpk(float lo, float hi) { f32x2 v = {lo, hi}; bf16x2_t b = __builtin_convertvector(v, bf16x2_t); return __builtin_bit_cast(unsigned, b); }
; template <int DQK, int DV, bool LEAD> ...
;     ...
; #pragma unroll
;           for (int ds = 0; ds < 2; ++ds)
; #pragma unroll
;               for (int j = 0; j < 8; ++j) x[ds][j] *= rn * qgain[32 * ds + 8 * g4 + j];
;           if constexpr (DQK == 64) {
; #pragma unroll
;               for (int ds = 0; ds < 2; ++ds)
; #pragma unroll
;                   for (int j = 0; j < 8; ++j) {
;                       auto rr = __builtin_amdgcn_permlane32_swap(__float_as_uint(x[ds][j]), __float_as_uint(x[ds][j]), false, false);
;                       const float other = hi ? __uint_as_float(rr[0]) : __uint_as_float(rr[1]);
;                       float cc = 1.f, sg = 0.f;
;                       if (lat) { const f32x2 cs = rope[(ds ? pcol : prow) * 16 + 8 * (g4 & 1) + j]; cc = cs.x; sg = hi ? cs.y : -cs.y; }
;                       x[ds][j] = x[ds][j] * cc + other * sg; }
;     ...
; #pragma unroll
;           for (int ds = 0; ds < NDS; ++ds) { u32x4 w;
; #pragma unroll
;               for (int i = 0; i < 4; ++i) w[i] = cvtpk(x[ds][2 * i] * c2, x[ds][2 * i + 1] * c2);
;               qf[qb * NDS + ds] = __builtin_bit_cast(bf16x8, w); }
	v_mov_b32_e32 v57, v13
	v_permlane32_swap_b32_e32 v15, v16
	s_nop 0
	v_permlane32_swap_b32_e32 v17, v57
	v_cndmask_b32_e32 v17, v17, v57, vcc
	v_cndmask_b32_e32 v16, v15, v16, vcc
	v_pk_mul_f32 v[16:17], v[128:129], v[16:17]
	s_nop 0
	v_pk_fma_f32 v[10:11], v[12:13], v[10:11], v[16:17]
	s_nop 0
	v_pk_mul_f32 v[10:11], v[10:11], s[94:95] op_sel_hi:[1,0]
	s_nop 0
	v_cvt_pk_bf16_f32 v13, v10, v11
	v_pk_mul_f32 v[10:11], v[58:59], v[56:57] op_sel_hi:[1,0]
	s_nop 0
	v_pk_mul_f32 v[10:11], v[10:11], v[134:135]
	s_nop 0
	v_mov_b32_e32 v12, v10
	v_mov_b32_e32 v15, v10
	v_mov_b32_e32 v16, v11
	v_mov_b32_e32 v17, v11
	v_permlane32_swap_b32_e32 v12, v15
	s_nop 0
	v_permlane32_swap_b32_e32 v16, v17
	v_cndmask_b32_e32 v17, v16, v17, vcc
	v_cndmask_b32_e32 v16, v12, v15, vcc
	v_pk_mul_f32 v[16:17], v[132:133], v[16:17]
	s_nop 0
	v_pk_fma_f32 v[10:11], v[10:11], v[92:93], v[16:17]
	v_and_b32_e32 v93, 0xffff0000, v14
	v_pk_mul_f32 v[10:11], v[10:11], s[94:95] op_sel_hi:[1,0]
	v_lshlrev_b32_e32 v92, 16, v14
	v_cvt_pk_bf16_f32 v12, v10, v11
	v_pk_mul_f32 v[10:11], v[64:65], v[56:57] op_sel_hi:[1,0]
	v_mul_f32_e32 v14, v93, v93
	v_pk_mul_f32 v[10:11], v[10:11], v[138:139]
	s_nop 0
	v_mov_b32_e32 v15, v10
	v_mov_b32_e32 v16, v10
	v_mov_b32_e32 v17, v11
	v_mov_b32_e32 v57, v11
	v_permlane32_swap_b32_e32 v15, v16
	s_nop 0
	v_permlane32_swap_b32_e32 v17, v57
	v_cndmask_b32_e32 v17, v17, v57, vcc
	v_cndmask_b32_e32 v16, v15, v16, vcc
	v_pk_mul_f32 v[16:17], v[136:137], v[16:17]
	s_nop 0
	v_pk_fma_f32 v[10:11], v[10:11], v[84:85], v[16:17]
	v_pk_mul_f32 v[16:17], v[62:63], v[56:57] op_sel_hi:[1,0]
	v_pk_mul_f32 v[10:11], v[10:11], s[94:95] op_sel_hi:[1,0]
	v_pk_mul_f32 v[16:17], v[16:17], v[140:141]
	v_cvt_pk_bf16_f32 v11, v10, v11
	v_mov_b32_e32 v10, v16
	v_mov_b32_e32 v15, v16
	v_mov_b32_e32 v57, v17
	v_mov_b32_e32 v81, v17
	v_permlane32_swap_b32_e32 v10, v15
	s_nop 0
	v_permlane32_swap_b32_e32 v57, v81
	v_cndmask_b32_e32 v85, v57, v81, vcc
	v_cndmask_b32_e32 v84, v10, v15, vcc
	v_pk_mul_f32 v[20:21], v[20:21], v[84:85]
	s_nop 0
	v_pk_fma_f32 v[16:17], v[16:17], v[88:89], v[20:21]
	v_mul_f32_e32 v88, v111, v111
	v_pk_mul_f32 v[16:17], v[16:17], s[94:95] op_sel_hi:[1,0]
	s_nop 0
	v_cvt_pk_bf16_f32 v10, v16, v17
	v_pk_mul_f32 v[16:17], v[74:75], v[56:57] op_sel_hi:[1,0]
	s_nop 0
	v_pk_mul_f32 v[16:17], v[16:17], v[142:143]
	s_nop 0
	v_mov_b32_e32 v15, v16
	v_mov_b32_e32 v20, v16
	v_mov_b32_e32 v21, v17
	v_mov_b32_e32 v57, v17
	v_permlane32_swap_b32_e32 v15, v20
	s_nop 0
	v_permlane32_swap_b32_e32 v21, v57
	v_cndmask_b32_e32 v21, v21, v57, vcc
	v_cndmask_b32_e32 v20, v15, v20, vcc
	v_pk_mul_f32 v[20:21], v[40:41], v[20:21]
	s_nop 0
	v_pk_fma_f32 v[16:17], v[16:17], v[42:43], v[20:21]
	v_pk_mul_f32 v[20:21], v[72:73], v[56:57] op_sel_hi:[1,0]
	v_pk_mul_f32 v[16:17], v[16:17], s[94:95] op_sel_hi:[1,0]
	v_pk_mul_f32 v[20:21], v[20:21], v[144:145]
	v_cvt_pk_bf16_f32 v17, v16, v17
	v_mov_b32_e32 v15, v20
	v_mov_b32_e32 v16, v20
	v_mov_b32_e32 v57, v21
	v_mov_b32_e32 v81, v21
	v_permlane32_swap_b32_e32 v15, v16
	s_nop 0
	v_permlane32_swap_b32_e32 v57, v81
	v_cndmask_b32_e32 v85, v57, v81, vcc
	v_cndmask_b32_e32 v84, v15, v16, vcc
	v_pk_mul_f32 v[84:85], v[44:45], v[84:85]
	s_nop 0
	v_pk_fma_f32 v[20:21], v[46:47], v[20:21], v[84:85]
	s_nop 0
	v_pk_mul_f32 v[20:21], v[20:21], s[94:95] op_sel_hi:[1,0]
	s_nop 0
	v_cvt_pk_bf16_f32 v16, v20, v21
	v_pk_mul_f32 v[20:21], v[78:79], v[56:57] op_sel_hi:[1,0]
	s_nop 0
	v_pk_mul_f32 v[20:21], v[20:21], v[148:149]
	s_nop 0
	v_mov_b32_e32 v15, v20
	v_mov_b32_e32 v57, v20
	v_mov_b32_e32 v81, v21
	v_mov_b32_e32 v84, v21
	v_permlane32_swap_b32_e32 v15, v57
	s_nop 0
	v_permlane32_swap_b32_e32 v81, v84
	v_cndmask_b32_e32 v85, v81, v84, vcc
	v_cndmask_b32_e32 v84, v15, v57, vcc
	v_pk_mul_f32 v[20:21], v[50:51], v[20:21]
	s_nop 0
	v_pk_fma_f32 v[20:21], v[48:49], v[84:85], v[20:21]
	s_nop 0
	v_pk_mul_f32 v[20:21], v[20:21], s[94:95] op_sel_hi:[1,0]
	s_nop 0
	v_cvt_pk_bf16_f32 v15, v20, v21
	v_pk_mul_f32 v[20:21], v[76:77], v[56:57] op_sel_hi:[1,0]
	v_pk_fma_f32 v[96:97], v[92:93], v[92:93], v[14:15] op_sel_hi:[1,1,0]
	v_pk_mul_f32 v[20:21], v[20:21], v[154:155]
	v_pk_fma_f32 v[96:97], v[52:53], v[52:53], v[96:97]
	v_mov_b32_e32 v56, v20
	v_mov_b32_e32 v81, v20
	s_nop 1
	v_permlane32_swap_b32_e32 v56, v81
	v_mov_b32_e32 v57, v21
	v_mov_b32_e32 v84, v21
	s_nop 1
	v_permlane32_swap_b32_e32 v57, v84
	v_cndmask_b32_e32 v56, v56, v81, vcc
	v_and_b32_e32 v81, 0xffff0000, v80
	v_cndmask_b32_e32 v57, v57, v84, vcc
	v_lshlrev_b32_e32 v80, 16, v80
	v_mul_f32_e32 v84, v81, v81
	v_pk_fma_f32 v[84:85], v[80:81], v[80:81], v[84:85] op_sel_hi:[1,1,0]
	v_mul_f32_e32 v14, v53, v53
	v_pk_fma_f32 v[84:85], v[110:111], v[110:111], v[84:85]
	v_pk_add_f32 v[96:97], v[14:15], v[96:97] op_sel_hi:[0,1]
	v_pk_add_f32 v[84:85], v[88:89], v[84:85] op_sel_hi:[0,1]
	v_pk_fma_f32 v[84:85], v[106:107], v[106:107], v[84:85]
	v_mul_f32_e32 v88, v107, v107
	v_pk_fma_f32 v[96:97], v[82:83], v[82:83], v[96:97]
	v_mul_f32_e32 v14, v83, v83
	v_pk_add_f32 v[84:85], v[88:89], v[84:85] op_sel_hi:[0,1]
	v_pk_add_f32 v[96:97], v[14:15], v[96:97] op_sel_hi:[0,1]
	v_pk_fma_f32 v[84:85], v[24:25], v[24:25], v[84:85]
	v_mul_f32_e32 v88, v25, v25
	v_pk_fma_f32 v[96:97], v[98:99], v[98:99], v[96:97]
	v_mul_f32_e32 v14, v99, v99
	v_pk_add_f32 v[84:85], v[88:89], v[84:85] op_sel_hi:[0,1]
	v_pk_add_f32 v[96:97], v[14:15], v[96:97] op_sel_hi:[0,1]
	v_pk_fma_f32 v[84:85], v[126:127], v[126:127], v[84:85]
	v_mul_f32_e32 v88, v127, v127
	v_pk_fma_f32 v[96:97], v[90:91], v[90:91], v[96:97]
	v_mul_f32_e32 v14, v91, v91
	v_pk_add_f32 v[84:85], v[88:89], v[84:85] op_sel_hi:[0,1]
; template <int DQK, int DV, bool LEAD> ...
;     ...
;           float sn = 0.f;
; #pragma unroll
;           for (int ds = 0; ds < 2; ++ds)
; #pragma unroll
;               for (int j = 0; j < 8; ++j) sn += x[ds][j] * x[ds][j];
;           sn = lanes4_sum(sn);
;           const float rn = rsqrtf(sn * (1.f / 64.f) + EPS);
; #pragma unroll
;           for (int ds = 0; ds < 2; ++ds)
; #pragma unroll
;               for (int j = 0; j < 8; ++j) x[ds][j] *= rn * qgain[32 * ds + 8 * g4 + j];
;           if constexpr (DQK == 64) {
; #pragma unroll
;               for (int ds = 0; ds < 2; ++ds)
; #pragma unroll
;                   for (int j = 0; j < 8; ++j) {
;                       auto rr = __builtin_amdgcn_permlane32_swap(__float_as_uint(x[ds][j]), __float_as_uint(x[ds][j]), false, false);
;                       const float other = hi ? __uint_as_float(rr[0]) : __uint_as_float(rr[1]);
;                       float cc = 1.f, sg = 0.f;
;                       if (lat) { const f32x2 cs = rope[(ds ? pcol : prow) * 16 + 8 * (g4 & 1) + j]; cc = cs.x; sg = hi ? cs.y : -cs.y; }
;                       x[ds][j] = x[ds][j] * cc + other * sg; }
	v_pk_add_f32 v[96:97], v[14:15], v[96:97] op_sel_hi:[0,1]
	v_pk_fma_f32 v[84:85], v[122:123], v[122:123], v[84:85]
	v_mul_f32_e32 v88, v123, v123
	v_pk_fma_f32 v[96:97], v[86:87], v[86:87], v[96:97]
	v_mul_f32_e32 v14, v87, v87
	v_pk_add_f32 v[84:85], v[88:89], v[84:85] op_sel_hi:[0,1]
	v_pk_add_f32 v[96:97], v[14:15], v[96:97] op_sel_hi:[0,1]
	v_pk_fma_f32 v[84:85], v[102:103], v[102:103], v[84:85]
	v_mul_f32_e32 v88, v103, v103
	v_pk_fma_f32 v[96:97], v[68:69], v[68:69], v[96:97]
	v_mul_f32_e32 v14, v69, v69
	v_pk_add_f32 v[84:85], v[88:89], v[84:85] op_sel_hi:[0,1]
	v_pk_add_f32 v[96:97], v[14:15], v[96:97] op_sel_hi:[0,1]
	v_pk_fma_f32 v[84:85], v[118:119], v[118:119], v[84:85]
	v_mul_f32_e32 v88, v119, v119
	v_pk_fma_f32 v[96:97], v[114:115], v[114:115], v[96:97]
	v_mul_f32_e32 v14, v115, v115
	v_pk_add_f32 v[84:85], v[88:89], v[84:85] op_sel_hi:[0,1]
	v_pk_add_f32 v[96:97], v[14:15], v[96:97] op_sel_hi:[0,1]
	v_mov_b32_e32 v85, v84
	v_mov_b32_e32 v14, v96
	s_nop 0
	v_permlane16_swap_b32_e32 v84, v85
	v_permlane16_swap_b32_e32 v96, v14
	v_add_f32_e32 v85, v84, v85
	v_add_f32_e32 v84, v96, v14
	v_mov_b32_e32 v89, v85
	v_mov_b32_e32 v88, v84
	s_nop 0
	v_permlane32_swap_b32_e32 v85, v89
	v_permlane32_swap_b32_e32 v84, v88
	v_pk_add_f32 v[84:85], v[84:85], v[88:89]
	v_pk_mul_f32 v[20:21], v[54:55], v[20:21]
	v_pk_fma_f32 v[84:85], v[84:85], s[12:13], v[108:109] op_sel_hi:[1,0,0]
	v_pk_fma_f32 v[20:21], v[104:105], v[56:57], v[20:21]
	v_mul_f32_e32 v14, 0x4b800000, v85
	v_cmp_gt_f32_e64 s[4:5], s95, v85
	v_pk_mul_f32 v[20:21], v[20:21], s[94:95] op_sel_hi:[1,0]
	s_nop 0
	v_cndmask_b32_e64 v14, v85, v14, s[4:5]
	v_rsq_f32_e32 v85, v14
	v_cvt_pk_bf16_f32 v14, v20, v21
	v_mul_f32_e32 v20, 0x45800000, v85
	v_cndmask_b32_e64 v56, v85, v20, s[4:5]
	v_pk_mul_f32 v[20:21], v[60:61], v[56:57] op_sel_hi:[1,0]
	v_cmp_gt_f32_e64 s[4:5], s95, v84
	v_pk_mul_f32 v[20:21], v[20:21], v[118:119]
	s_nop 0
	v_mov_b32_e32 v57, v20
	v_mov_b32_e32 v85, v20
	v_mov_b32_e32 v88, v21
	v_mov_b32_e32 v89, v21
	v_permlane32_swap_b32_e32 v57, v85
	s_nop 0
	v_permlane32_swap_b32_e32 v88, v89
	v_cndmask_b32_e32 v89, v88, v89, vcc
	v_cndmask_b32_e32 v88, v57, v85, vcc
	v_pk_mul_f32 v[88:89], v[116:117], v[88:89]
	s_nop 0
	v_pk_fma_f32 v[20:21], v[20:21], v[70:71], v[88:89]
	v_pk_mul_f32 v[70:71], v[58:59], v[56:57] op_sel_hi:[1,0]
	v_pk_mul_f32 v[20:21], v[20:21], s[94:95] op_sel_hi:[1,0]
	v_pk_mul_f32 v[70:71], v[70:71], v[102:103]
	v_cvt_pk_bf16_f32 v21, v20, v21
	v_mov_b32_e32 v20, v70
	v_mov_b32_e32 v57, v70
	v_mov_b32_e32 v85, v71
	v_mov_b32_e32 v88, v71
	v_permlane32_swap_b32_e32 v20, v57
	s_nop 0
	v_permlane32_swap_b32_e32 v85, v88
	v_cndmask_b32_e32 v89, v85, v88, vcc
	v_cndmask_b32_e32 v88, v20, v57, vcc
	v_pk_mul_f32 v[88:89], v[94:95], v[88:89]
	s_nop 0
	v_pk_fma_f32 v[66:67], v[70:71], v[66:67], v[88:89]
	s_nop 0
	v_pk_mul_f32 v[66:67], v[66:67], s[94:95] op_sel_hi:[1,0]
	s_nop 0
	v_cvt_pk_bf16_f32 v20, v66, v67
	v_pk_mul_f32 v[66:67], v[64:65], v[56:57] op_sel_hi:[1,0]
	s_nop 0
	v_pk_mul_f32 v[66:67], v[66:67], v[122:123]
	s_nop 0
	v_mov_b32_e32 v57, v66
	v_mov_b32_e32 v70, v66
	v_mov_b32_e32 v71, v67
	v_mov_b32_e32 v85, v67
	v_permlane32_swap_b32_e32 v57, v70
	s_nop 0
	v_permlane32_swap_b32_e32 v71, v85
	v_cndmask_b32_e32 v71, v71, v85, vcc
	v_cndmask_b32_e32 v70, v57, v70, vcc
	v_pk_mul_f32 v[70:71], v[120:121], v[70:71]
	s_nop 0
	v_pk_fma_f32 v[18:19], v[66:67], v[18:19], v[70:71]
	v_pk_mul_f32 v[66:67], v[62:63], v[56:57] op_sel_hi:[1,0]
	v_pk_mul_f32 v[18:19], v[18:19], s[94:95] op_sel_hi:[1,0]
	v_pk_mul_f32 v[66:67], v[66:67], v[126:127]
	v_cvt_pk_bf16_f32 v19, v18, v19
	v_mov_b32_e32 v18, v66
	v_mov_b32_e32 v57, v66
	v_mov_b32_e32 v70, v67
	v_mov_b32_e32 v71, v67
	v_permlane32_swap_b32_e32 v18, v57
	s_nop 0
	v_permlane32_swap_b32_e32 v70, v71
	v_cndmask_b32_e32 v71, v70, v71, vcc
	v_cndmask_b32_e32 v70, v18, v57, vcc
	v_pk_mul_f32 v[70:71], v[124:125], v[70:71]
	s_nop 0
	v_pk_fma_f32 v[22:23], v[66:67], v[22:23], v[70:71]
	s_nop 0
	v_pk_mul_f32 v[22:23], v[22:23], s[94:95] op_sel_hi:[1,0]
	s_nop 0
	v_cvt_pk_bf16_f32 v18, v22, v23
	v_pk_mul_f32 v[22:23], v[74:75], v[56:57] op_sel_hi:[1,0]
	s_nop 0
	v_pk_mul_f32 v[22:23], v[22:23], v[24:25]
	s_nop 0
	v_mov_b32_e32 v24, v22
	v_mov_b32_e32 v57, v22
	v_mov_b32_e32 v25, v23
	v_mov_b32_e32 v66, v23
	v_permlane32_swap_b32_e32 v24, v57
	s_nop 0
	v_permlane32_swap_b32_e32 v25, v66
	v_cndmask_b32_e32 v25, v25, v66, vcc
	v_cndmask_b32_e32 v24, v24, v57, vcc
	v_pk_mul_f32 v[24:25], v[40:41], v[24:25]
	s_nop 0
	v_pk_fma_f32 v[22:23], v[22:23], v[42:43], v[24:25]
	s_nop 0
	v_pk_mul_f32 v[22:23], v[22:23], s[94:95] op_sel_hi:[1,0]
	s_nop 0
	v_cvt_pk_bf16_f32 v25, v22, v23
	v_pk_mul_f32 v[22:23], v[72:73], v[56:57] op_sel_hi:[1,0]
	s_nop 0
	v_pk_mul_f32 v[22:23], v[22:23], v[106:107]
	s_nop 0
	v_mov_b32_e32 v24, v22
	v_mov_b32_e32 v57, v22
	v_mov_b32_e32 v66, v23
	v_mov_b32_e32 v67, v23
	v_permlane32_swap_b32_e32 v24, v57
	s_nop 0
	v_permlane32_swap_b32_e32 v66, v67
	v_cndmask_b32_e32 v67, v66, v67, vcc
	v_cndmask_b32_e32 v66, v24, v57, vcc
	v_pk_mul_f32 v[66:67], v[44:45], v[66:67]
	s_nop 0
	v_pk_fma_f32 v[22:23], v[46:47], v[22:23], v[66:67]
	s_nop 0
	v_pk_mul_f32 v[22:23], v[22:23], s[94:95] op_sel_hi:[1,0]
	s_nop 0
	v_cvt_pk_bf16_f32 v24, v22, v23
	v_pk_mul_f32 v[22:23], v[78:79], v[56:57] op_sel_hi:[1,0]
	s_nop 0
	v_pk_mul_f32 v[22:23], v[22:23], v[110:111]
	s_nop 0
	v_mov_b32_e32 v57, v22
	v_mov_b32_e32 v66, v22
	v_mov_b32_e32 v67, v23
	v_mov_b32_e32 v70, v23
	v_permlane32_swap_b32_e32 v57, v66
	s_nop 0
	v_permlane32_swap_b32_e32 v67, v70
	v_cndmask_b32_e32 v67, v67, v70, vcc
	v_cndmask_b32_e32 v66, v57, v66, vcc
; __device__ __forceinline__ unsigned cvtpk(float lo, float hi) { f32x2 v = {lo, hi}; bf16x2_t b = __builtin_convertvector(v, bf16x2_t); return __builtin_bit_cast(unsigned, b); }
; template <int DQK, int DV, bool LEAD> ...
;     ...
;               for (int ds = 0; ds < 2; ++ds)
; #pragma unroll
;                   for (int j = 0; j < 8; ++j) {
;                       auto rr = __builtin_amdgcn_permlane32_swap(__float_as_uint(x[ds][j]), __float_as_uint(x[ds][j]), false, false);
;                       const float other = hi ? __uint_as_float(rr[0]) : __uint_as_float(rr[1]);
;                       float cc = 1.f, sg = 0.f;
;                       if (lat) { const f32x2 cs = rope[(ds ? pcol : prow) * 16 + 8 * (g4 & 1) + j]; cc = cs.x; sg = hi ? cs.y : -cs.y; }
;                       x[ds][j] = x[ds][j] * cc + other * sg; }
;           } else {
;               float sr = 0.f;
; #pragma unroll
;               for (int j = 0; j < 8; ++j) sr += x[2][j] * x[2][j];
;               sr = lanes4_sum(sr);
;               const float rq = rsqrtf(sr * (1.f / 32.f) + EPS);
; #pragma unroll
;               for (int j = 0; j < 8; ++j) { const float av = x[2][j] * rq * qgain[64 + 8 * g4 + j];
;                   auto rr = __builtin_amdgcn_permlane16_swap(__float_as_uint(av), __float_as_uint(av), false, false);
;                   const float other = (g4 & 1) ? __uint_as_float(rr[0]) : __uint_as_float(rr[1]);
;                   float cc = 1.f, sg = 0.f;
;                   if (lat) { const f32x2 cs = rope[((g4 & 2) ? pcol : prow) * 8 + j]; cc = cs.x; sg = (g4 & 1) ? cs.y : -cs.y; }
;                   x[2][j] = av * cc + other * sg; }
;           }
; #pragma unroll
;           for (int ds = 0; ds < NDS; ++ds) { u32x4 w;
; #pragma unroll
;               for (int i = 0; i < 4; ++i) w[i] = cvtpk(x[ds][2 * i] * c2, x[ds][2 * i + 1] * c2);
;               qf[qb * NDS + ds] = __builtin_bit_cast(bf16x8, w); }
;       }
; #pragma unroll
;       for (int d0 = 0; d0 < NQB * NDS; ++d0) asm volatile("" : "+v"(qf[d0])); }
;     wait_bar<0>();
;     bf16x8 kf[NKW * NDS], vf[NVF];
;     ATT_KLOAD(0);
;     asm volatile("s_waitcnt lgkmcnt(0)\n\ts_barrier" ::: "memory");
	v_pk_mul_f32 v[22:23], v[50:51], v[22:23]
	v_pk_mul_f32 v[56:57], v[76:77], v[56:57] op_sel_hi:[1,0]
	v_pk_fma_f32 v[22:23], v[48:49], v[66:67], v[22:23]
	v_pk_mul_f32 v[56:57], v[56:57], v[80:81]
	v_pk_mul_f32 v[22:23], v[22:23], s[94:95] op_sel_hi:[1,0]
	v_mov_b32_e32 v66, v56
	v_cvt_pk_bf16_f32 v23, v22, v23
	v_mov_b32_e32 v22, v56
	s_nop 1
	v_permlane32_swap_b32_e32 v22, v66
	v_mov_b32_e32 v67, v57
	v_mov_b32_e32 v70, v57
	v_cndmask_b32_e32 v66, v22, v66, vcc
	v_mul_f32_e32 v22, 0x4b800000, v84
	v_permlane32_swap_b32_e32 v67, v70
	v_cndmask_b32_e64 v22, v84, v22, s[4:5]
	v_cndmask_b32_e32 v67, v67, v70, vcc
	v_rsq_f32_e32 v70, v22
	v_pk_mul_f32 v[56:57], v[54:55], v[56:57]
	s_nop 0
	v_pk_fma_f32 v[56:57], v[104:105], v[66:67], v[56:57]
	s_nop 0
	v_pk_mul_f32 v[56:57], v[56:57], s[94:95] op_sel_hi:[1,0]
	s_nop 0
	v_cvt_pk_bf16_f32 v22, v56, v57
	v_mul_f32_e32 v56, 0x45800000, v70
	v_cndmask_b32_e64 v56, v70, v56, s[4:5]
	v_pk_mul_f32 v[66:67], v[76:77], v[56:57] op_sel_hi:[1,0]
	v_pk_mul_f32 v[70:71], v[78:79], v[56:57] op_sel_hi:[1,0]
	v_pk_mul_f32 v[66:67], v[66:67], v[92:93]
	v_pk_mul_f32 v[58:59], v[58:59], v[56:57] op_sel_hi:[1,0]
	v_pk_mul_f32 v[52:53], v[70:71], v[52:53]
	v_pk_mul_f32 v[70:71], v[72:73], v[56:57] op_sel_hi:[1,0]
	v_pk_mul_f32 v[72:73], v[74:75], v[56:57] op_sel_hi:[1,0]
	v_pk_mul_f32 v[62:63], v[62:63], v[56:57] op_sel_hi:[1,0]
	v_pk_mul_f32 v[64:65], v[64:65], v[56:57] op_sel_hi:[1,0]
	v_pk_mul_f32 v[58:59], v[58:59], v[68:69]
	v_pk_mul_f32 v[56:57], v[60:61], v[56:57] op_sel_hi:[1,0]
	v_mov_b32_e32 v60, v66
	v_mov_b32_e32 v68, v66
	v_mov_b32_e32 v61, v67
	v_mov_b32_e32 v69, v67
	v_permlane32_swap_b32_e32 v60, v68
	s_nop 0
	v_permlane32_swap_b32_e32 v61, v69
	v_cndmask_b32_e32 v61, v61, v69, vcc
	v_cndmask_b32_e32 v60, v60, v68, vcc
	v_pk_mul_f32 v[54:55], v[54:55], v[66:67]
	v_mov_b32_e32 v66, v52
	v_pk_fma_f32 v[54:55], v[104:105], v[60:61], v[54:55]
	v_mov_b32_e32 v60, v52
	v_mov_b32_e32 v61, v53
	v_mov_b32_e32 v67, v53
	v_permlane32_swap_b32_e32 v60, v66
	s_nop 0
	v_permlane32_swap_b32_e32 v61, v67
	v_pk_mul_f32 v[70:71], v[70:71], v[82:83]
	v_cndmask_b32_e32 v61, v61, v67, vcc
	v_cndmask_b32_e32 v60, v60, v66, vcc
	v_pk_mul_f32 v[50:51], v[50:51], v[52:53]
	v_mov_b32_e32 v52, v70
	v_pk_fma_f32 v[48:49], v[48:49], v[60:61], v[50:51]
	v_mov_b32_e32 v50, v70
	v_mov_b32_e32 v51, v71
	v_mov_b32_e32 v53, v71
	v_permlane32_swap_b32_e32 v50, v52
	s_nop 0
	v_permlane32_swap_b32_e32 v51, v53
	v_cndmask_b32_e32 v51, v51, v53, vcc
	v_cndmask_b32_e32 v50, v50, v52, vcc
	v_pk_mul_f32 v[72:73], v[72:73], v[98:99]
	v_pk_mul_f32 v[44:45], v[44:45], v[50:51]
	v_mov_b32_e32 v50, v72
	v_pk_fma_f32 v[44:45], v[46:47], v[70:71], v[44:45]
	v_mov_b32_e32 v46, v72
	v_mov_b32_e32 v47, v73
	v_mov_b32_e32 v51, v73
	v_permlane32_swap_b32_e32 v46, v50
	s_nop 0
	v_permlane32_swap_b32_e32 v47, v51
	v_cndmask_b32_e32 v47, v47, v51, vcc
	v_cndmask_b32_e32 v46, v46, v50, vcc
	v_pk_mul_f32 v[62:63], v[62:63], v[90:91]
	v_pk_mul_f32 v[40:41], v[40:41], v[46:47]
	v_mov_b32_e32 v46, v62
	v_pk_fma_f32 v[40:41], v[72:73], v[42:43], v[40:41]
	v_mov_b32_e32 v42, v62
	v_mov_b32_e32 v43, v63
	v_mov_b32_e32 v47, v63
	v_permlane32_swap_b32_e32 v42, v46
	s_nop 0
	v_permlane32_swap_b32_e32 v43, v47
	v_cndmask_b32_e32 v43, v43, v47, vcc
	v_cndmask_b32_e32 v42, v42, v46, vcc
	v_pk_mul_f32 v[64:65], v[64:65], v[86:87]
	v_pk_mul_f32 v[36:37], v[36:37], v[42:43]
	v_mov_b32_e32 v42, v64
	v_pk_fma_f32 v[36:37], v[62:63], v[38:39], v[36:37]
	v_mov_b32_e32 v38, v64
	v_mov_b32_e32 v39, v65
	v_mov_b32_e32 v43, v65
	v_permlane32_swap_b32_e32 v38, v42
	s_nop 0
	v_permlane32_swap_b32_e32 v39, v43
	v_cndmask_b32_e32 v39, v39, v43, vcc
	v_cndmask_b32_e32 v38, v38, v42, vcc
	v_pk_mul_f32 v[32:33], v[32:33], v[38:39]
	v_mov_b32_e32 v38, v58
	v_pk_fma_f32 v[32:33], v[64:65], v[34:35], v[32:33]
	v_mov_b32_e32 v34, v58
	v_mov_b32_e32 v35, v59
	v_mov_b32_e32 v39, v59
	v_permlane32_swap_b32_e32 v34, v38
	s_nop 0
	v_permlane32_swap_b32_e32 v35, v39
	v_cndmask_b32_e32 v35, v35, v39, vcc
	v_cndmask_b32_e32 v34, v34, v38, vcc
	v_pk_mul_f32 v[56:57], v[56:57], v[114:115]
	v_pk_mul_f32 v[28:29], v[28:29], v[34:35]
	v_pk_mul_f32 v[32:33], v[32:33], s[94:95] op_sel_hi:[1,0]
	v_pk_fma_f32 v[34:35], v[58:59], v[30:31], v[28:29]
	v_mov_b32_e32 v28, v56
	v_mov_b32_e32 v30, v56
	v_mov_b32_e32 v29, v57
	v_mov_b32_e32 v31, v57
	v_permlane32_swap_b32_e32 v28, v30
	s_nop 0
	v_permlane32_swap_b32_e32 v29, v31
	v_cndmask_b32_e32 v29, v29, v31, vcc
	v_cndmask_b32_e32 v28, v28, v30, vcc
	v_pk_mul_f32 v[28:29], v[112:113], v[28:29]
	v_pk_mul_f32 v[30:31], v[40:41], s[94:95] op_sel_hi:[1,0]
	v_pk_fma_f32 v[38:39], v[56:57], v[26:27], v[28:29]
	v_pk_mul_f32 v[26:27], v[54:55], s[94:95] op_sel_hi:[1,0]
	v_pk_mul_f32 v[28:29], v[48:49], s[94:95] op_sel_hi:[1,0]
	v_cvt_pk_bf16_f32 v26, v26, v27
	v_cvt_pk_bf16_f32 v27, v28, v29
	v_pk_mul_f32 v[28:29], v[44:45], s[94:95] op_sel_hi:[1,0]
	v_bfe_u32 v54, v168, 1, 3
	v_cvt_pk_bf16_f32 v28, v28, v29
	v_cvt_pk_bf16_f32 v29, v30, v31
	v_pk_mul_f32 v[30:31], v[36:37], s[94:95] op_sel_hi:[1,0]
	v_bitop3_b32 v54, v171, v54, 4 bitop3:0x36
	v_cvt_pk_bf16_f32 v30, v30, v31
	v_cvt_pk_bf16_f32 v31, v32, v33
	v_pk_mul_f32 v[32:33], v[34:35], s[94:95] op_sel_hi:[1,0]
	v_pk_mul_f32 v[34:35], v[38:39], s[94:95] op_sel_hi:[1,0]
	v_cvt_pk_bf16_f32 v32, v32, v33
	v_cvt_pk_bf16_f32 v33, v34, v35
	s_waitcnt vmcnt(0) lgkmcnt(0)
	s_barrier
	ds_read_b128 v[34:37], v175
	ds_read_b128 v[38:41], v175 offset:512
	v_lshlrev_b32_e32 v82, 4, v54
	v_add_u32_e32 v178, v169, v82
	s_waitcnt lgkmcnt(1)
	v_mfma_f32_16x16x32_bf16 v[42:45], v[34:37], v[6:9], 0
	ds_read_b128 v[54:57], v178
	ds_read_b128 v[58:61], v178 offset:512
	s_waitcnt lgkmcnt(0)
	s_barrier
; #define ATT_SB() __builtin_amdgcn_sched_barrier(0)
; #define ATT_DMA_K(t, sl) do { glds16(ksrc + (size_t)(t) * 64 * kpitch, (unsigned)__builtin_amdgcn_readfirstlane(kdst + (sl) * KSLOT)); \
;         if constexpr (DQK == 96) glds16(krsrc + (size_t)(t) * 64 * 32, (unsigned)__builtin_amdgcn_readfirstlane(krdst + (sl) * KSLOT)); } while (0)
; #define ATT_DMA_V(t, sl) do { glds16(vsrc + (size_t)(t) * 64, (unsigned)__builtin_amdgcn_readfirstlane(vdst + (sl) * VSLOT)); \
;         if constexpr (DV == 128) glds16(vsrc + (size_t)64 * NR + (size_t)(t) * 64, (unsigned)__builtin_amdgcn_readfirstlane(vdst + (sl) * VSLOT + 8192)); } while (0)
; #define ATT_KLOAD(sl) do { _Pragma("unroll") for (int kb_ = 0; kb_ < NKW; ++kb_) _Pragma("unroll") for (int ds_ = 0; ds_ < NDS; ++ds_) { \
;         if (ds_ < 2) kf[kb_ * NDS + ds_] = *(const LAS bf16x8*)(kp[ds_ & 1] + (sl) * KSLOT + (kb_ & 1) * 512 + (kb_ >> 1) * 4096); \
;         else kf[kb_ * NDS + ds_] = *(const LAS bf16x8*)(krp + (sl) * KSLOT + (kb_ & 1) * 256 + (kb_ >> 1) * 2048); } } while (0)
; #define ATT_QK() do { _Pragma("unroll") for (int kb_ = 0; kb_ < NKW; ++kb_) _Pragma("unroll") for (int ds_ = 0; ds_ < NDS; ++ds_) _Pragma("unroll") for (int qb_ = 0; qb_ < NQB; ++qb_) \
;         c[kb_][qb_] = __builtin_amdgcn_mfma_f32_16x16x32_bf16(kf[kb_ * NDS + ds_], qf[qb_ * NDS + ds_], ds_ == 0 ? zero4 : c[kb_][qb_], 0, 0, 0); } while (0)
; #define ATT_EXP() do { _Pragma("unroll") for (int kb_ = 0; kb_ < NKW; ++kb_) _Pragma("unroll") for (int qb_ = 0; qb_ < NQB; ++qb_) _Pragma("unroll") for (int i_ = 0; i_ < 4; ++i_) \
;         c[kb_][qb_][i_] = __builtin_amdgcn_exp2f(c[kb_][qb_][i_]); } while (0)
; template <int DQK, int DV, bool LEAD> ...
;     ...
;     const f32x4 zero4 = {0.f, 0.f, 0.f, 0.f};
;     f32x4 o[NDB][NQB], c[NKW][NQB]; u32x4 pw[4];
; #pragma unroll
;     for (int i = 0; i < NDB; ++i)
; #pragma unroll
;         for (int qb = 0; qb < NQB; ++qb) o[i][qb] = zero4;
;     ATT_DMA_K(3, 0); ATT_DMA_V(1, 1);
;     ATT_QK(); ATT_SB();
;     ATT_KLOAD(1); ATT_SB();
;     if constexpr (LEAD) { ATT_EXP(); ATT_SUMPACK(); }
;     wait_bar<NDMA>();
;     int s_prev = 0, s_cur = 1, s_next = 2;
	s_cselect_b64 vcc, -1, 0
	v_mfma_f32_16x16x32_bf16 v[46:49], v[34:37], v[14:17], 0
	v_mfma_f32_16x16x32_bf16 v[50:53], v[34:37], v[22:25], 0
	v_mfma_f32_16x16x32_bf16 v[34:37], v[34:37], v[26:29], 0
	s_waitcnt lgkmcnt(1)
	v_mfma_f32_16x16x32_bf16 v[62:65], v[54:57], v[2:5], v[42:45]
	v_mfma_f32_16x16x32_bf16 v[66:69], v[54:57], v[10:13], v[46:49]
	v_mfma_f32_16x16x32_bf16 v[50:53], v[54:57], v[18:21], v[50:53]
	v_mfma_f32_16x16x32_bf16 v[54:57], v[54:57], v[30:33], v[34:37]
	v_mfma_f32_16x16x32_bf16 v[34:37], v[38:41], v[6:9], 0
	v_mfma_f32_16x16x32_bf16 v[42:45], v[38:41], v[14:17], 0
	v_mfma_f32_16x16x32_bf16 v[46:49], v[38:41], v[22:25], 0
	v_mfma_f32_16x16x32_bf16 v[38:41], v[38:41], v[26:29], 0
	s_waitcnt lgkmcnt(0)
	v_mfma_f32_16x16x32_bf16 v[70:73], v[58:61], v[2:5], v[34:37]
	v_mfma_f32_16x16x32_bf16 v[74:77], v[58:61], v[10:13], v[42:45]
	s_nop 1
	v_lshl_add_u64 v[34:35], v[162:163], 0, s[96:97]
	s_mov_b32 s4, m0
	s_mov_b32 m0, s49
	s_nop 0
	global_load_lds_dwordx4 v[34:35], off
	s_mov_b32 m0, s4
	v_lshl_add_u64 v[34:35], v[164:165], 0, s[66:67]
	v_mfma_f32_16x16x32_bf16 v[78:81], v[58:61], v[18:21], v[46:49]
	s_add_i32 s4, s36, 0x2000
	s_mov_b32 s5, m0
	s_mov_b32 m0, s4
	s_nop 0
	global_load_lds_dwordx4 v[34:35], off
	s_mov_b32 m0, s5
	v_mfma_f32_16x16x32_bf16 v[58:61], v[58:61], v[30:33], v[38:41]
	ds_read_b128 v[34:37], v175 offset:8192
	s_nop 1
	ds_read_b128 v[38:41], v175 offset:8704
	ds_read_b128 v[42:45], v178 offset:8192
	ds_read_b128 v[46:49], v178 offset:8704
	v_exp_f32_e32 v62, v62
	v_exp_f32_e32 v63, v63
	v_exp_f32_e32 v64, v64
	v_exp_f32_e32 v65, v65
	v_exp_f32_e32 v66, v66
	v_exp_f32_e32 v67, v67
	v_exp_f32_e32 v68, v68
	v_exp_f32_e32 v69, v69
	v_exp_f32_e32 v83, v50
	v_exp_f32_e32 v84, v51
	v_exp_f32_e32 v85, v52
	v_exp_f32_e32 v86, v53
	v_exp_f32_e32 v54, v54
	v_exp_f32_e32 v55, v55
	v_exp_f32_e32 v56, v56
	v_exp_f32_e32 v57, v57
	v_add_f32_e32 v50, v62, v63
	v_add_f32_e32 v51, v64, v65
	v_exp_f32_e32 v70, v70
	v_exp_f32_e32 v74, v74
	v_exp_f32_e32 v78, v78
	v_exp_f32_e32 v58, v58
	v_add_f32_e32 v50, v50, v51
	v_add_f32_e32 v51, v66, v67
	v_add_f32_e32 v52, v68, v69
	v_add_f32_e32 v51, v51, v52
	v_add_f32_e32 v52, v83, v84
	v_add_f32_e32 v53, v85, v86
	v_exp_f32_e32 v71, v71
	v_exp_f32_e32 v75, v75
	v_exp_f32_e32 v79, v79
	v_exp_f32_e32 v59, v59
	v_add_f32_e32 v52, v52, v53
	v_add_f32_e32 v53, v54, v55
	v_add_f32_e32 v87, v56, v57
	v_add_f32_e32 v53, v53, v87
	v_exp_f32_e32 v72, v72
	v_exp_f32_e32 v76, v76
	v_exp_f32_e32 v80, v80
	v_exp_f32_e32 v60, v60
	v_add_f32_e32 v50, v50, v70
	v_add_f32_e32 v51, v51, v74
	v_add_f32_e32 v52, v52, v78
	v_add_f32_e32 v53, v53, v58
	v_exp_f32_e32 v73, v73
	v_exp_f32_e32 v77, v77
	v_exp_f32_e32 v81, v81
	v_exp_f32_e32 v61, v61
	v_add_f32_e32 v50, v71, v50
	v_add_f32_e32 v51, v75, v51
	v_add_f32_e32 v52, v79, v52
	v_add_f32_e32 v53, v59, v53
	s_mov_b32 s4, 1
	v_add_f32_e32 v50, v72, v50
	v_add_f32_e32 v87, v76, v51
	v_add_f32_e32 v52, v80, v52
	v_add_f32_e32 v88, v60, v53
	v_cvt_pk_bf16_f32 v102, v62, v63
	v_add_f32_e32 v51, v73, v50
	v_add_f32_e32 v50, v77, v87
	v_add_f32_e32 v53, v81, v52
	v_add_f32_e32 v52, v61, v88
	s_waitcnt vmcnt(2) lgkmcnt(0)
	s_barrier
	s_cmp_lg_u32 s4, 0
	v_pk_add_f32 v[168:169], v[50:51], 0 op_sel_hi:[1,0]
	v_cndmask_b32_e32 v50, v82, v177, vcc
	v_add3_u32 v177, 0, v173, v50
	v_mov_b32_e32 v50, 0
	v_pk_add_f32 v[166:167], v[52:53], 0 op_sel_hi:[1,0]
	v_cvt_pk_bf16_f32 v103, v64, v65
	v_cvt_pk_bf16_f32 v104, v70, v71
	v_cvt_pk_bf16_f32 v105, v72, v73
	v_cvt_pk_bf16_f32 v114, v66, v67
	v_cvt_pk_bf16_f32 v115, v68, v69
	v_cvt_pk_bf16_f32 v116, v74, v75
	v_cvt_pk_bf16_f32 v117, v76, v77
	v_cvt_pk_bf16_f32 v122, v83, v84
	v_cvt_pk_bf16_f32 v123, v85, v86
	v_cvt_pk_bf16_f32 v124, v78, v79
	v_cvt_pk_bf16_f32 v125, v80, v81
	v_cvt_pk_bf16_f32 v126, v54, v55
	v_cvt_pk_bf16_f32 v127, v56, v57
	v_cvt_pk_bf16_f32 v128, v58, v59
	v_cvt_pk_bf16_f32 v129, v60, v61
	s_cselect_b64 s[4:5], -1, 0
	s_mov_b32 s37, 2
	v_mov_b32_e32 v51, v50
	v_mov_b32_e32 v52, v50
	v_mov_b32_e32 v53, v50
	v_mov_b32_e32 v54, v50
	v_mov_b32_e32 v55, v50
	v_mov_b32_e32 v56, v50
	v_mov_b32_e32 v57, v50
	v_mov_b32_e32 v58, v50
	v_mov_b32_e32 v59, v50
	v_mov_b32_e32 v60, v50
	v_mov_b32_e32 v61, v50
	v_mov_b32_e32 v62, v50
	v_mov_b32_e32 v63, v50
	v_mov_b32_e32 v64, v50
	v_mov_b32_e32 v65, v50
	v_mov_b32_e32 v66, v50
	v_mov_b32_e32 v67, v50
	v_mov_b32_e32 v68, v50
	v_mov_b32_e32 v69, v50
	v_mov_b32_e32 v70, v50
	v_mov_b32_e32 v71, v50
	v_mov_b32_e32 v72, v50
	v_mov_b32_e32 v73, v50
	v_mov_b32_e32 v74, v50
	v_mov_b32_e32 v75, v50
	v_mov_b32_e32 v76, v50
	v_mov_b32_e32 v77, v50
	v_mov_b32_e32 v78, v50
	v_mov_b32_e32 v79, v50
	v_mov_b32_e32 v80, v50
	v_mov_b32_e32 v81, v50
	v_mov_b32_e32 v82, v50
	v_mov_b32_e32 v83, v50
	v_mov_b32_e32 v84, v50
	v_mov_b32_e32 v85, v50
	v_mov_b32_e32 v86, v50
	v_mov_b32_e32 v87, v50
	v_mov_b32_e32 v88, v50
	v_mov_b32_e32 v89, v50
	v_mov_b32_e32 v90, v50
	v_mov_b32_e32 v91, v50
	v_mov_b32_e32 v92, v50
	v_mov_b32_e32 v93, v50
	v_mov_b32_e32 v94, v50
	v_mov_b32_e32 v95, v50
	v_mov_b32_e32 v96, v50
	v_mov_b32_e32 v97, v50
	v_mov_b32_e32 v98, v50
	v_mov_b32_e32 v99, v50
	v_mov_b32_e32 v100, v50
	v_mov_b32_e32 v101, v50
	v_mov_b32_e32 v106, v50
	v_mov_b32_e32 v107, v50
	v_mov_b32_e32 v108, v50
	v_mov_b32_e32 v109, v50
	v_mov_b32_e32 v110, v50
	v_mov_b32_e32 v111, v50
	v_mov_b32_e32 v112, v50
	v_mov_b32_e32 v113, v50
	v_mov_b32_e32 v118, v50
	v_mov_b32_e32 v119, v50
	v_mov_b32_e32 v120, v50
	v_mov_b32_e32 v121, v50
	s_branch .LBB0_965
